# GEMM unit loops: accumulator zero-init with v_mov_b64 (65 instead of 128 moves) on top of the MFMA segment head trim
# speedup vs baseline: 1.0088x; 1.0045x over previous
; #define PG8_STAGE(bufoff, gbase, voff) do { _Pragma("unroll") for (int _i = 0; _i < 2; ++_i) \
;         __builtin_amdgcn_global_load_lds((const unsigned*)((const char*)(gbase) + (voff)[_i]), (PG8_LAS unsigned*)(lds + (bufoff) + ldsw + _i * 8192), 16, 0, 0); } while (0)
; #define PG8_WAIT_V(n) asm volatile("s_waitcnt vmcnt(" #n ")" ::: "memory")
;     ...
;         const char* nA = has_next ? S.a_base(nxt) : cA; const char* nB = has_next ? S.b_base(nxt) : cB;
;         for (int t = 0; t < nt; t += 2) {
;             const bool last = (t == nt - 2);
;             const char* a1 = cA + (size_t)(t + 1) * kstep;
;             const char* a2 = last ? nA : cA + (size_t)(t + 2) * kstep; const char* b2 = last ? nB : cB + (size_t)(t + 2) * kstep;
;             const char* a3 = a2 + kstep; const char* b3 = b2 + kstep;
;             if (last && has_next) S.a_ready(nxt);
;             PG8_LDB(B0, 0, 0); PG8_LDB(B1, 0, 1); PG8_SCHED; PG8_LDA(At, 0, 0); PG8_STAGE(PG8_SA(1, 1), a1 + hstep, voffA);
;             PG8_WAIT_V(8); PG8_WAIT_L(0); PG8_BAR; PG8_MMA(0, 0, At, B0); PG8_MMA(0, 1, At, B1); PG8_BAR; PG8_SCHED;
;             PG8_LDA(At, 0, 1); PG8_STAGE(PG8_SB(0, 0), b2, voffB); PG8_STAGE(PG8_SB(0, 1), b2 + hstep, voffB); PG8_STAGE(PG8_SA(0, 0), a2, voffA);
;             PG8_WAIT_V(8); PG8_WAIT_L(0); PG8_BAR; PG8_MMA(1, 0, At, B0); PG8_MMA(1, 1, At, B1); PG8_BAR; PG8_SCHED;
;             PG8_LDB(B0, 1, 0); PG8_LDB(B1, 1, 1); PG8_SCHED; PG8_LDA(At, 1, 0); PG8_STAGE(PG8_SA(0, 1), a2 + hstep, voffA);
;             PG8_WAIT_V(8); PG8_WAIT_L(0); PG8_BAR; PG8_MMA(0, 0, At, B0); PG8_MMA(0, 1, At, B1); PG8_BAR; PG8_SCHED;
;             PG8_LDA(At, 1, 1); PG8_STAGE(PG8_SB(1, 0), b3, voffB); PG8_STAGE(PG8_SB(1, 1), b3 + hstep, voffB); PG8_STAGE(PG8_SA(1, 0), a3, voffA);
;             PG8_WAIT_V(8); PG8_WAIT_L(0); PG8_BAR; PG8_MMA(1, 0, At, B0); PG8_MMA(1, 1, At, B1); PG8_BAR; PG8_SCHED;
;         }
;         if constexpr (ALIGN_EPI) { if (wr == 0) PG8_BAR; }
;         E(acc, cur, wr, wc, fr, fq); S.done(cur);
;         if (!has_next) break;
; #pragma unroll
;         for (int a = 0; a < 2; ++a)
; #pragma unroll
;             for (int b = 0; b < 2; ++b)
; #pragma unroll
;                 for (int m = 0; m < 4; ++m)
; #pragma unroll
;                     for (int n = 0; n < 2; ++n) acc[a][b][m][n] = (f32x4){0.f, 0.f, 0.f, 0.f};
;         cur = nxt; cA = nA; cB = nB; ++ui;
.LBB0_189:
	s_ashr_i32 s17, s16, 31
	s_lshl_b64 s[20:21], s[16:17], 19
	s_cmpk_gt_i32 s14, 0x3e7
	s_cselect_b32 s15, s28, s30
	s_cselect_b32 s0, s29, s31
	s_add_u32 s20, s15, s20
	s_addc_u32 s21, s0, s21
	s_and_b64 s[26:27], s[26:27], exec
	s_cselect_b32 s0, s21, s25
	s_cselect_b32 s15, s20, s24
	s_add_u32 s22, s22, 0x40080
	s_addc_u32 s23, s23, 0
	s_add_u32 s17, s24, 0x100
	v_mov_b32_e32 v2, 0
	s_addc_u32 s45, s25, 0
	s_mov_b32 s46, -2
	v_mov_b32_e32 v3, v2
	v_mov_b64_e32 v[4:5], v[2:3]
	v_mov_b64_e32 v[6:7], v[2:3]
	v_mov_b64_e32 v[8:9], v[2:3]
	v_mov_b64_e32 v[10:11], v[2:3]
	v_mov_b64_e32 v[12:13], v[2:3]
	v_mov_b64_e32 v[14:15], v[2:3]
	v_mov_b64_e32 v[16:17], v[2:3]
	v_mov_b64_e32 v[18:19], v[2:3]
	v_mov_b64_e32 v[20:21], v[2:3]
	v_mov_b64_e32 v[22:23], v[2:3]
	v_mov_b64_e32 v[24:25], v[2:3]
	v_mov_b64_e32 v[26:27], v[2:3]
	v_mov_b64_e32 v[28:29], v[2:3]
	v_mov_b64_e32 v[30:31], v[2:3]
	v_mov_b64_e32 v[32:33], v[2:3]
	v_mov_b64_e32 v[34:35], v[2:3]
	v_mov_b64_e32 v[36:37], v[2:3]
	v_mov_b64_e32 v[38:39], v[2:3]
	v_mov_b64_e32 v[40:41], v[2:3]
	v_mov_b64_e32 v[42:43], v[2:3]
	v_mov_b64_e32 v[44:45], v[2:3]
	v_mov_b64_e32 v[46:47], v[2:3]
	v_mov_b64_e32 v[48:49], v[2:3]
	v_mov_b64_e32 v[50:51], v[2:3]
	v_mov_b64_e32 v[52:53], v[2:3]
	v_mov_b64_e32 v[54:55], v[2:3]
	v_mov_b64_e32 v[56:57], v[2:3]
	v_mov_b64_e32 v[58:59], v[2:3]
	v_mov_b64_e32 v[60:61], v[2:3]
	v_mov_b64_e32 v[62:63], v[2:3]
	v_mov_b64_e32 v[64:65], v[2:3]
	v_mov_b64_e32 v[66:67], v[2:3]
	v_mov_b64_e32 v[68:69], v[2:3]
	v_mov_b64_e32 v[70:71], v[2:3]
	v_mov_b64_e32 v[72:73], v[2:3]
	v_mov_b64_e32 v[74:75], v[2:3]
	v_mov_b64_e32 v[76:77], v[2:3]
	v_mov_b64_e32 v[78:79], v[2:3]
	v_mov_b64_e32 v[80:81], v[2:3]
	v_mov_b64_e32 v[82:83], v[2:3]
	v_mov_b64_e32 v[84:85], v[2:3]
	v_mov_b64_e32 v[86:87], v[2:3]
	v_mov_b64_e32 v[88:89], v[2:3]
	v_mov_b64_e32 v[90:91], v[2:3]
	v_mov_b64_e32 v[92:93], v[2:3]
	v_mov_b64_e32 v[94:95], v[2:3]
	v_mov_b64_e32 v[96:97], v[2:3]
	v_mov_b64_e32 v[98:99], v[2:3]
	v_mov_b64_e32 v[100:101], v[2:3]
	v_mov_b64_e32 v[102:103], v[2:3]
	v_mov_b64_e32 v[104:105], v[2:3]
	v_mov_b64_e32 v[106:107], v[2:3]
	v_mov_b64_e32 v[108:109], v[2:3]
	v_mov_b64_e32 v[110:111], v[2:3]
	v_mov_b64_e32 v[112:113], v[2:3]
	v_mov_b64_e32 v[114:115], v[2:3]
	v_mov_b64_e32 v[116:117], v[2:3]
	v_mov_b64_e32 v[118:119], v[2:3]
	v_mov_b64_e32 v[120:121], v[2:3]
	v_mov_b64_e32 v[122:123], v[2:3]
	v_mov_b64_e32 v[124:125], v[2:3]
	v_mov_b64_e32 v[126:127], v[2:3]
	v_mov_b64_e32 v[128:129], v[2:3]

;     __device__ __forceinline__ bool next(int i, Unit& u) const { return unit_of((long)i * G + c, u); }
;     __device__ __forceinline__ bool next(int i, Unit& u) const { if (i >= 64) return false; return unit_of((long)__builtin_amdgcn_readfirstlane(list[i]), u); }
;     ...
;         const bool has_next = S.next(ui + 1, nxt);
;         const char* nA = has_next ? S.a_base(nxt) : cA; const char* nB = has_next ? S.b_base(nxt) : cB;
;         for (int t = 0; t < nt; t += 2) {
;             const bool last = (t == nt - 2);
;             const char* a1 = cA + (size_t)(t + 1) * kstep;
;             const char* a2 = last ? nA : cA + (size_t)(t + 2) * kstep; const char* b2 = last ? nB : cB + (size_t)(t + 2) * kstep;
;             const char* a3 = a2 + kstep; const char* b3 = b2 + kstep;
;     ...
;         for (int a = 0; a < 2; ++a)
; #pragma unroll
;             for (int b = 0; b < 2; ++b)
; #pragma unroll
;                 for (int m = 0; m < 4; ++m)
; #pragma unroll
;                     for (int n = 0; n < 2; ++n) acc[a][b][m][n] = (f32x4){0.f, 0.f, 0.f, 0.f};
;         cur = nxt; cA = nA; cB = nB; ++ui;
.LBB0_840:
	s_ashr_i32 s11, s10, 31
	s_lshl_b64 s[12:13], s[10:11], 19
	s_add_u32 s12, s24, s12
	s_addc_u32 s13, s25, s13
	s_and_b64 s[14:15], s[4:5], exec
	s_cselect_b32 s11, s13, s19
	s_cselect_b32 s17, s12, s18
	s_ashr_i32 s9, s8, 31
	s_lshl_b64 s[14:15], s[8:9], 19
	s_add_u32 s14, s26, s14
	s_addc_u32 s15, s27, s15
	s_and_b64 s[22:23], s[4:5], exec
	s_cselect_b32 s9, s15, s21
	s_cselect_b32 s47, s14, s20
	s_add_u32 s18, s18, 0x40080
	s_addc_u32 s19, s19, 0
	s_add_u32 s48, s20, 0x100
	v_mov_b32_e32 v2, 0
	s_addc_u32 s49, s21, 0
	s_mov_b32 s50, -2
	v_mov_b32_e32 v3, v2
	v_mov_b64_e32 v[4:5], v[2:3]
	v_mov_b64_e32 v[6:7], v[2:3]
	v_mov_b64_e32 v[8:9], v[2:3]
	v_mov_b64_e32 v[10:11], v[2:3]
	v_mov_b64_e32 v[12:13], v[2:3]
	v_mov_b64_e32 v[14:15], v[2:3]
	v_mov_b64_e32 v[16:17], v[2:3]
	v_mov_b64_e32 v[18:19], v[2:3]
	v_mov_b64_e32 v[20:21], v[2:3]
	v_mov_b64_e32 v[22:23], v[2:3]
	v_mov_b64_e32 v[24:25], v[2:3]
	v_mov_b64_e32 v[26:27], v[2:3]
	v_mov_b64_e32 v[28:29], v[2:3]
	v_mov_b64_e32 v[30:31], v[2:3]
	v_mov_b64_e32 v[32:33], v[2:3]
	v_mov_b64_e32 v[34:35], v[2:3]
	v_mov_b64_e32 v[36:37], v[2:3]
	v_mov_b64_e32 v[38:39], v[2:3]
	v_mov_b64_e32 v[40:41], v[2:3]
	v_mov_b64_e32 v[42:43], v[2:3]
	v_mov_b64_e32 v[44:45], v[2:3]
	v_mov_b64_e32 v[46:47], v[2:3]
	v_mov_b64_e32 v[48:49], v[2:3]
	v_mov_b64_e32 v[50:51], v[2:3]
	v_mov_b64_e32 v[52:53], v[2:3]
	v_mov_b64_e32 v[54:55], v[2:3]
	v_mov_b64_e32 v[56:57], v[2:3]
	v_mov_b64_e32 v[58:59], v[2:3]
	v_mov_b64_e32 v[60:61], v[2:3]
	v_mov_b64_e32 v[62:63], v[2:3]
	v_mov_b64_e32 v[64:65], v[2:3]
	v_mov_b64_e32 v[66:67], v[2:3]
	v_mov_b64_e32 v[68:69], v[2:3]
	v_mov_b64_e32 v[70:71], v[2:3]
	v_mov_b64_e32 v[72:73], v[2:3]
	v_mov_b64_e32 v[74:75], v[2:3]
	v_mov_b64_e32 v[76:77], v[2:3]
	v_mov_b64_e32 v[78:79], v[2:3]
	v_mov_b64_e32 v[80:81], v[2:3]
	v_mov_b64_e32 v[82:83], v[2:3]
	v_mov_b64_e32 v[84:85], v[2:3]
	v_mov_b64_e32 v[86:87], v[2:3]
	v_mov_b64_e32 v[88:89], v[2:3]
	v_mov_b64_e32 v[90:91], v[2:3]
	v_mov_b64_e32 v[92:93], v[2:3]
	v_mov_b64_e32 v[94:95], v[2:3]
	v_mov_b64_e32 v[96:97], v[2:3]
	v_mov_b64_e32 v[98:99], v[2:3]
	v_mov_b64_e32 v[100:101], v[2:3]
	v_mov_b64_e32 v[102:103], v[2:3]
	v_mov_b64_e32 v[104:105], v[2:3]
	v_mov_b64_e32 v[106:107], v[2:3]
	v_mov_b64_e32 v[108:109], v[2:3]
	v_mov_b64_e32 v[110:111], v[2:3]
	v_mov_b64_e32 v[112:113], v[2:3]
	v_mov_b64_e32 v[114:115], v[2:3]
	v_mov_b64_e32 v[116:117], v[2:3]
	v_mov_b64_e32 v[118:119], v[2:3]
	v_mov_b64_e32 v[120:121], v[2:3]
	v_mov_b64_e32 v[122:123], v[2:3]
	v_mov_b64_e32 v[124:125], v[2:3]
	v_mov_b64_e32 v[126:127], v[2:3]
	v_mov_b64_e32 v[128:129], v[2:3]

;     __device__ __forceinline__ bool next(int i, Unit& u) const { return unit_of((long)i * G + c, u); }
;     __device__ __forceinline__ bool next(int i, Unit& u) const { if (i >= 64) return false; return unit_of((long)__builtin_amdgcn_readfirstlane(list[i]), u); }
;     ...
;         const bool has_next = S.next(ui + 1, nxt);
;         const char* nA = has_next ? S.a_base(nxt) : cA; const char* nB = has_next ? S.b_base(nxt) : cB;
;         for (int t = 0; t < nt; t += 2) {
;             const bool last = (t == nt - 2);
;             const char* a1 = cA + (size_t)(t + 1) * kstep;
;             const char* a2 = last ? nA : cA + (size_t)(t + 2) * kstep; const char* b2 = last ? nB : cB + (size_t)(t + 2) * kstep;
;             const char* a3 = a2 + kstep; const char* b3 = b2 + kstep;
;     ...
;         for (int a = 0; a < 2; ++a)
; #pragma unroll
;             for (int b = 0; b < 2; ++b)
; #pragma unroll
;                 for (int m = 0; m < 4; ++m)
; #pragma unroll
;                     for (int n = 0; n < 2; ++n) acc[a][b][m][n] = (f32x4){0.f, 0.f, 0.f, 0.f};
;         cur = nxt; cA = nA; cB = nB; ++ui;
.LBB0_994:
	s_ashr_i32 s13, s12, 31
	s_lshl_b64 s[14:15], s[12:13], 19
	s_add_u32 s14, s26, s14
	s_addc_u32 s15, s27, s15
	s_and_b64 s[16:17], s[4:5], exec
	s_cselect_b32 s13, s15, s21
	s_cselect_b32 s49, s14, s20
	s_ashr_i32 s11, s10, 31
	s_lshl_b64 s[16:17], s[10:11], 19
	s_add_u32 s16, s28, s16
	s_addc_u32 s17, s29, s17
	s_and_b64 s[24:25], s[4:5], exec
	s_cselect_b32 s11, s17, s23
	s_cselect_b32 s50, s16, s22
	s_add_u32 s20, s20, 0x40080
	s_addc_u32 s21, s21, 0
	s_add_u32 s51, s22, 0x100
	v_mov_b32_e32 v2, 0
	s_addc_u32 s52, s23, 0
	s_mov_b32 s53, -2
	v_mov_b32_e32 v3, v2
	v_mov_b64_e32 v[4:5], v[2:3]
	v_mov_b64_e32 v[6:7], v[2:3]
	v_mov_b64_e32 v[8:9], v[2:3]
	v_mov_b64_e32 v[10:11], v[2:3]
	v_mov_b64_e32 v[12:13], v[2:3]
	v_mov_b64_e32 v[14:15], v[2:3]
	v_mov_b64_e32 v[16:17], v[2:3]
	v_mov_b64_e32 v[18:19], v[2:3]
	v_mov_b64_e32 v[20:21], v[2:3]
	v_mov_b64_e32 v[22:23], v[2:3]
	v_mov_b64_e32 v[24:25], v[2:3]
	v_mov_b64_e32 v[26:27], v[2:3]
	v_mov_b64_e32 v[28:29], v[2:3]
	v_mov_b64_e32 v[30:31], v[2:3]
	v_mov_b64_e32 v[32:33], v[2:3]
	v_mov_b64_e32 v[34:35], v[2:3]
	v_mov_b64_e32 v[36:37], v[2:3]
	v_mov_b64_e32 v[38:39], v[2:3]
	v_mov_b64_e32 v[40:41], v[2:3]
	v_mov_b64_e32 v[42:43], v[2:3]
	v_mov_b64_e32 v[44:45], v[2:3]
	v_mov_b64_e32 v[46:47], v[2:3]
	v_mov_b64_e32 v[48:49], v[2:3]
	v_mov_b64_e32 v[50:51], v[2:3]
	v_mov_b64_e32 v[52:53], v[2:3]
	v_mov_b64_e32 v[54:55], v[2:3]
	v_mov_b64_e32 v[56:57], v[2:3]
	v_mov_b64_e32 v[58:59], v[2:3]
	v_mov_b64_e32 v[60:61], v[2:3]
	v_mov_b64_e32 v[62:63], v[2:3]
	v_mov_b64_e32 v[64:65], v[2:3]
	v_mov_b64_e32 v[66:67], v[2:3]
	v_mov_b64_e32 v[68:69], v[2:3]
	v_mov_b64_e32 v[70:71], v[2:3]
	v_mov_b64_e32 v[72:73], v[2:3]
	v_mov_b64_e32 v[74:75], v[2:3]
	v_mov_b64_e32 v[76:77], v[2:3]
	v_mov_b64_e32 v[78:79], v[2:3]
	v_mov_b64_e32 v[80:81], v[2:3]
	v_mov_b64_e32 v[82:83], v[2:3]
	v_mov_b64_e32 v[84:85], v[2:3]
	v_mov_b64_e32 v[86:87], v[2:3]
	v_mov_b64_e32 v[88:89], v[2:3]
	v_mov_b64_e32 v[90:91], v[2:3]
	v_mov_b64_e32 v[92:93], v[2:3]
	v_mov_b64_e32 v[94:95], v[2:3]
	v_mov_b64_e32 v[96:97], v[2:3]
	v_mov_b64_e32 v[98:99], v[2:3]
	v_mov_b64_e32 v[100:101], v[2:3]
	v_mov_b64_e32 v[102:103], v[2:3]
	v_mov_b64_e32 v[104:105], v[2:3]
	v_mov_b64_e32 v[106:107], v[2:3]
	v_mov_b64_e32 v[108:109], v[2:3]
	v_mov_b64_e32 v[110:111], v[2:3]
	v_mov_b64_e32 v[112:113], v[2:3]
	v_mov_b64_e32 v[114:115], v[2:3]
	v_mov_b64_e32 v[116:117], v[2:3]
	v_mov_b64_e32 v[118:119], v[2:3]
	v_mov_b64_e32 v[120:121], v[2:3]
	v_mov_b64_e32 v[122:123], v[2:3]
	v_mov_b64_e32 v[124:125], v[2:3]
	v_mov_b64_e32 v[126:127], v[2:3]
	v_mov_b64_e32 v[128:129], v[2:3]

;     ...
;             const char* a1 = cA + (size_t)(t + 1) * kstep;
;             const char* a2 = last ? nA : cA + (size_t)(t + 2) * kstep; const char* b2 = last ? nB : cB + (size_t)(t + 2) * kstep;
;             const char* a3 = a2 + kstep; const char* b3 = b2 + kstep;
;     ...
;         for (int a = 0; a < 2; ++a)
; #pragma unroll
;             for (int b = 0; b < 2; ++b)
; #pragma unroll
;                 for (int m = 0; m < 4; ++m)
; #pragma unroll
;                     for (int n = 0; n < 2; ++n) acc[a][b][m][n] = (f32x4){0.f, 0.f, 0.f, 0.f};
;         cur = nxt; cA = nA; cB = nB; ++ui;
.LBB0_1116:
	s_add_u32 s14, s14, 0xb0080
	s_addc_u32 s15, s15, 0
	s_add_u32 s0, s16, 0x100
	v_mov_b32_e32 v2, 0
	s_addc_u32 s47, s17, 0
	s_mov_b32 s48, -2
	v_mov_b32_e32 v3, v2
	v_mov_b64_e32 v[4:5], v[2:3]
	v_mov_b64_e32 v[6:7], v[2:3]
	v_mov_b64_e32 v[8:9], v[2:3]
	v_mov_b64_e32 v[10:11], v[2:3]
	v_mov_b64_e32 v[12:13], v[2:3]
	v_mov_b64_e32 v[14:15], v[2:3]
	v_mov_b64_e32 v[16:17], v[2:3]
	v_mov_b64_e32 v[18:19], v[2:3]
	v_mov_b64_e32 v[20:21], v[2:3]
	v_mov_b64_e32 v[22:23], v[2:3]
	v_mov_b64_e32 v[24:25], v[2:3]
	v_mov_b64_e32 v[26:27], v[2:3]
	v_mov_b64_e32 v[28:29], v[2:3]
	v_mov_b64_e32 v[30:31], v[2:3]
	v_mov_b64_e32 v[32:33], v[2:3]
	v_mov_b64_e32 v[34:35], v[2:3]
	v_mov_b64_e32 v[36:37], v[2:3]
	v_mov_b64_e32 v[38:39], v[2:3]
	v_mov_b64_e32 v[40:41], v[2:3]
	v_mov_b64_e32 v[42:43], v[2:3]
	v_mov_b64_e32 v[44:45], v[2:3]
	v_mov_b64_e32 v[46:47], v[2:3]
	v_mov_b64_e32 v[48:49], v[2:3]
	v_mov_b64_e32 v[50:51], v[2:3]
	v_mov_b64_e32 v[52:53], v[2:3]
	v_mov_b64_e32 v[54:55], v[2:3]
	v_mov_b64_e32 v[56:57], v[2:3]
	v_mov_b64_e32 v[58:59], v[2:3]
	v_mov_b64_e32 v[60:61], v[2:3]
	v_mov_b64_e32 v[62:63], v[2:3]
	v_mov_b64_e32 v[64:65], v[2:3]
	v_mov_b64_e32 v[66:67], v[2:3]
	v_mov_b64_e32 v[68:69], v[2:3]
	v_mov_b64_e32 v[70:71], v[2:3]
	v_mov_b64_e32 v[72:73], v[2:3]
	v_mov_b64_e32 v[74:75], v[2:3]
	v_mov_b64_e32 v[76:77], v[2:3]
	v_mov_b64_e32 v[78:79], v[2:3]
	v_mov_b64_e32 v[80:81], v[2:3]
	v_mov_b64_e32 v[82:83], v[2:3]
	v_mov_b64_e32 v[84:85], v[2:3]
	v_mov_b64_e32 v[86:87], v[2:3]
	v_mov_b64_e32 v[88:89], v[2:3]
	v_mov_b64_e32 v[90:91], v[2:3]
	v_mov_b64_e32 v[92:93], v[2:3]
	v_mov_b64_e32 v[94:95], v[2:3]
	v_mov_b64_e32 v[96:97], v[2:3]
	v_mov_b64_e32 v[98:99], v[2:3]
	v_mov_b64_e32 v[100:101], v[2:3]
	v_mov_b64_e32 v[102:103], v[2:3]
	v_mov_b64_e32 v[104:105], v[2:3]
	v_mov_b64_e32 v[106:107], v[2:3]
	v_mov_b64_e32 v[108:109], v[2:3]
	v_mov_b64_e32 v[110:111], v[2:3]
	v_mov_b64_e32 v[112:113], v[2:3]
	v_mov_b64_e32 v[114:115], v[2:3]
	v_mov_b64_e32 v[116:117], v[2:3]
	v_mov_b64_e32 v[118:119], v[2:3]
	v_mov_b64_e32 v[120:121], v[2:3]
	v_mov_b64_e32 v[122:123], v[2:3]
	v_mov_b64_e32 v[124:125], v[2:3]
	v_mov_b64_e32 v[126:127], v[2:3]
	v_mov_b64_e32 v[128:129], v[2:3]

;     ...
;             const char* a1 = cA + (size_t)(t + 1) * kstep;
;             const char* a2 = last ? nA : cA + (size_t)(t + 2) * kstep; const char* b2 = last ? nB : cB + (size_t)(t + 2) * kstep;
;             const char* a3 = a2 + kstep; const char* b3 = b2 + kstep;
;     ...
;         for (int a = 0; a < 2; ++a)
; #pragma unroll
;             for (int b = 0; b < 2; ++b)
; #pragma unroll
;                 for (int m = 0; m < 4; ++m)
; #pragma unroll
;                     for (int n = 0; n < 2; ++n) acc[a][b][m][n] = (f32x4){0.f, 0.f, 0.f, 0.f};
;         cur = nxt; cA = nA; cB = nB; ++ui;
.LBB0_2241:
	s_add_u32 s74, s74, 0xe0080
	v_lshl_add_u64 v[164:165], v[2:3], 0, s[88:89]
	v_mov_b32_e32 v2, 0
	s_addc_u32 s75, s75, 0
	s_mov_b32 s19, -2
	v_mov_b32_e32 v3, v2
	v_mov_b64_e32 v[4:5], v[2:3]
	v_mov_b64_e32 v[6:7], v[2:3]
	v_mov_b64_e32 v[8:9], v[2:3]
	v_mov_b64_e32 v[10:11], v[2:3]
	v_mov_b64_e32 v[12:13], v[2:3]
	v_mov_b64_e32 v[14:15], v[2:3]
	v_mov_b64_e32 v[16:17], v[2:3]
	v_mov_b64_e32 v[18:19], v[2:3]
	v_mov_b64_e32 v[20:21], v[2:3]
	v_mov_b64_e32 v[22:23], v[2:3]
	v_mov_b64_e32 v[24:25], v[2:3]
	v_mov_b64_e32 v[26:27], v[2:3]
	v_mov_b64_e32 v[28:29], v[2:3]
	v_mov_b64_e32 v[30:31], v[2:3]
	v_mov_b64_e32 v[32:33], v[2:3]
	v_mov_b64_e32 v[34:35], v[2:3]
	v_mov_b64_e32 v[36:37], v[2:3]
	v_mov_b64_e32 v[38:39], v[2:3]
	v_mov_b64_e32 v[40:41], v[2:3]
	v_mov_b64_e32 v[42:43], v[2:3]
	v_mov_b64_e32 v[44:45], v[2:3]
	v_mov_b64_e32 v[46:47], v[2:3]
	v_mov_b64_e32 v[48:49], v[2:3]
	v_mov_b64_e32 v[50:51], v[2:3]
	v_mov_b64_e32 v[52:53], v[2:3]
	v_mov_b64_e32 v[54:55], v[2:3]
	v_mov_b64_e32 v[56:57], v[2:3]
	v_mov_b64_e32 v[58:59], v[2:3]
	v_mov_b64_e32 v[60:61], v[2:3]
	v_mov_b64_e32 v[62:63], v[2:3]
	v_mov_b64_e32 v[64:65], v[2:3]
	v_mov_b64_e32 v[66:67], v[2:3]
	v_mov_b64_e32 v[68:69], v[2:3]
	v_mov_b64_e32 v[70:71], v[2:3]
	v_mov_b64_e32 v[72:73], v[2:3]
	v_mov_b64_e32 v[74:75], v[2:3]
	v_mov_b64_e32 v[76:77], v[2:3]
	v_mov_b64_e32 v[78:79], v[2:3]
	v_mov_b64_e32 v[80:81], v[2:3]
	v_mov_b64_e32 v[82:83], v[2:3]
	v_mov_b64_e32 v[84:85], v[2:3]
	v_mov_b64_e32 v[86:87], v[2:3]
	v_mov_b64_e32 v[88:89], v[2:3]
	v_mov_b64_e32 v[90:91], v[2:3]
	v_mov_b64_e32 v[92:93], v[2:3]
	v_mov_b64_e32 v[94:95], v[2:3]
	v_mov_b64_e32 v[96:97], v[2:3]
	v_mov_b64_e32 v[98:99], v[2:3]
	v_mov_b64_e32 v[100:101], v[2:3]
	v_mov_b64_e32 v[102:103], v[2:3]
	v_mov_b64_e32 v[104:105], v[2:3]
	v_mov_b64_e32 v[106:107], v[2:3]
	v_mov_b64_e32 v[108:109], v[2:3]
	v_mov_b64_e32 v[110:111], v[2:3]
	v_mov_b64_e32 v[112:113], v[2:3]
	v_mov_b64_e32 v[114:115], v[2:3]
	v_mov_b64_e32 v[116:117], v[2:3]
	v_mov_b64_e32 v[118:119], v[2:3]
	v_mov_b64_e32 v[120:121], v[2:3]
	v_mov_b64_e32 v[122:123], v[2:3]
	v_mov_b64_e32 v[124:125], v[2:3]
	v_mov_b64_e32 v[126:127], v[2:3]
	v_mov_b64_e32 v[128:129], v[2:3]

;     __device__ __forceinline__ bool next(int i, Unit& u) const { return unit_of((long)i * G + c, u); }
;     __device__ __forceinline__ bool next(int i, Unit& u) const { if (i >= 64) return false; return unit_of((long)__builtin_amdgcn_readfirstlane(list[i]), u); }
;     ...
;         const bool has_next = S.next(ui + 1, nxt);
;         const char* nA = has_next ? S.a_base(nxt) : cA; const char* nB = has_next ? S.b_base(nxt) : cB;
;         for (int t = 0; t < nt; t += 2) {
;             const bool last = (t == nt - 2);
;             const char* a1 = cA + (size_t)(t + 1) * kstep;
;             const char* a2 = last ? nA : cA + (size_t)(t + 2) * kstep; const char* b2 = last ? nB : cB + (size_t)(t + 2) * kstep;
;             const char* a3 = a2 + kstep; const char* b3 = b2 + kstep;
;     ...
;         for (int a = 0; a < 2; ++a)
; #pragma unroll
;             for (int b = 0; b < 2; ++b)
; #pragma unroll
;                 for (int m = 0; m < 4; ++m)
; #pragma unroll
;                     for (int n = 0; n < 2; ++n) acc[a][b][m][n] = (f32x4){0.f, 0.f, 0.f, 0.f};
;         cur = nxt; cA = nA; cB = nB; ++ui;
.LBB0_2270:
	s_ashr_i32 s75, s74, 31
	s_lshl_b64 s[0:1], s[74:75], 19
	s_add_u32 s0, s44, s0
	s_addc_u32 s1, s45, s1
	s_and_b64 s[16:17], s[46:47], exec
	s_cselect_b32 s15, s1, s93
	s_cselect_b32 s16, s0, s92
	s_add_u32 s92, s92, 0x40080
	v_lshl_add_u64 v[164:165], v[2:3], 0, s[88:89]
	v_mov_b32_e32 v2, 0
	s_addc_u32 s93, s93, 0
	s_mov_b32 s17, -2
	v_mov_b32_e32 v3, v2
	v_mov_b64_e32 v[4:5], v[2:3]
	v_mov_b64_e32 v[6:7], v[2:3]
	v_mov_b64_e32 v[8:9], v[2:3]
	v_mov_b64_e32 v[10:11], v[2:3]
	v_mov_b64_e32 v[12:13], v[2:3]
	v_mov_b64_e32 v[14:15], v[2:3]
	v_mov_b64_e32 v[16:17], v[2:3]
	v_mov_b64_e32 v[18:19], v[2:3]
	v_mov_b64_e32 v[20:21], v[2:3]
	v_mov_b64_e32 v[22:23], v[2:3]
	v_mov_b64_e32 v[24:25], v[2:3]
	v_mov_b64_e32 v[26:27], v[2:3]
	v_mov_b64_e32 v[28:29], v[2:3]
	v_mov_b64_e32 v[30:31], v[2:3]
	v_mov_b64_e32 v[32:33], v[2:3]
	v_mov_b64_e32 v[34:35], v[2:3]
	v_mov_b64_e32 v[36:37], v[2:3]
	v_mov_b64_e32 v[38:39], v[2:3]
	v_mov_b64_e32 v[40:41], v[2:3]
	v_mov_b64_e32 v[42:43], v[2:3]
	v_mov_b64_e32 v[44:45], v[2:3]
	v_mov_b64_e32 v[46:47], v[2:3]
	v_mov_b64_e32 v[48:49], v[2:3]
	v_mov_b64_e32 v[50:51], v[2:3]
	v_mov_b64_e32 v[52:53], v[2:3]
	v_mov_b64_e32 v[54:55], v[2:3]
	v_mov_b64_e32 v[56:57], v[2:3]
	v_mov_b64_e32 v[58:59], v[2:3]
	v_mov_b64_e32 v[60:61], v[2:3]
	v_mov_b64_e32 v[62:63], v[2:3]
	v_mov_b64_e32 v[64:65], v[2:3]
	v_mov_b64_e32 v[66:67], v[2:3]
	v_mov_b64_e32 v[68:69], v[2:3]
	v_mov_b64_e32 v[70:71], v[2:3]
	v_mov_b64_e32 v[72:73], v[2:3]
	v_mov_b64_e32 v[74:75], v[2:3]
	v_mov_b64_e32 v[76:77], v[2:3]
	v_mov_b64_e32 v[78:79], v[2:3]
	v_mov_b64_e32 v[80:81], v[2:3]
	v_mov_b64_e32 v[82:83], v[2:3]
	v_mov_b64_e32 v[84:85], v[2:3]
	v_mov_b64_e32 v[86:87], v[2:3]
	v_mov_b64_e32 v[88:89], v[2:3]
	v_mov_b64_e32 v[90:91], v[2:3]
	v_mov_b64_e32 v[92:93], v[2:3]
	v_mov_b64_e32 v[94:95], v[2:3]
	v_mov_b64_e32 v[96:97], v[2:3]
	v_mov_b64_e32 v[98:99], v[2:3]
	v_mov_b64_e32 v[100:101], v[2:3]
	v_mov_b64_e32 v[102:103], v[2:3]
	v_mov_b64_e32 v[104:105], v[2:3]
	v_mov_b64_e32 v[106:107], v[2:3]
	v_mov_b64_e32 v[108:109], v[2:3]
	v_mov_b64_e32 v[110:111], v[2:3]
	v_mov_b64_e32 v[112:113], v[2:3]
	v_mov_b64_e32 v[114:115], v[2:3]
	v_mov_b64_e32 v[116:117], v[2:3]
	v_mov_b64_e32 v[118:119], v[2:3]
	v_mov_b64_e32 v[120:121], v[2:3]
	v_mov_b64_e32 v[122:123], v[2:3]
	v_mov_b64_e32 v[124:125], v[2:3]
	v_mov_b64_e32 v[126:127], v[2:3]
	v_mov_b64_e32 v[128:129], v[2:3]

;     __device__ __forceinline__ bool next(int i, Unit& u) const { return unit_of((long)i * G + c, u); }
;     __device__ __forceinline__ bool next(int i, Unit& u) const { if (i >= 64) return false; return unit_of((long)__builtin_amdgcn_readfirstlane(list[i]), u); }
;     ...
;         const bool has_next = S.next(ui + 1, nxt);
;         const char* nA = has_next ? S.a_base(nxt) : cA; const char* nB = has_next ? S.b_base(nxt) : cB;
;         for (int t = 0; t < nt; t += 2) {
;             const bool last = (t == nt - 2);
;             const char* a1 = cA + (size_t)(t + 1) * kstep;
;             const char* a2 = last ? nA : cA + (size_t)(t + 2) * kstep; const char* b2 = last ? nB : cB + (size_t)(t + 2) * kstep;
;             const char* a3 = a2 + kstep; const char* b3 = b2 + kstep;
;     ...
;         for (int a = 0; a < 2; ++a)
; #pragma unroll
;             for (int b = 0; b < 2; ++b)
; #pragma unroll
;                 for (int m = 0; m < 4; ++m)
; #pragma unroll
;                     for (int n = 0; n < 2; ++n) acc[a][b][m][n] = (f32x4){0.f, 0.f, 0.f, 0.f};
;         cur = nxt; cA = nA; cB = nB; ++ui;
.LBB0_3247:
	s_ashr_i32 s13, s12, 31
	s_lshl_b64 s[14:15], s[12:13], 19
	s_add_u32 s14, s26, s14
	s_addc_u32 s15, s27, s15
	s_and_b64 s[16:17], s[4:5], exec
	s_cselect_b32 s13, s15, s21
	s_cselect_b32 s51, s14, s20
	s_ashr_i32 s11, s10, 31
	s_lshl_b64 s[16:17], s[10:11], 19
	s_add_u32 s16, s28, s16
	s_addc_u32 s17, s29, s17
	s_and_b64 s[24:25], s[4:5], exec
	s_cselect_b32 s11, s17, s23
	s_cselect_b32 s52, s16, s22
	s_add_u32 s20, s20, 0x40080
	s_addc_u32 s21, s21, 0
	s_add_u32 s53, s22, 0x100
	v_mov_b32_e32 v2, 0
	s_addc_u32 s54, s23, 0
	s_mov_b32 s55, -2
	v_mov_b32_e32 v3, v2
	v_mov_b64_e32 v[4:5], v[2:3]
	v_mov_b64_e32 v[6:7], v[2:3]
	v_mov_b64_e32 v[8:9], v[2:3]
	v_mov_b64_e32 v[10:11], v[2:3]
	v_mov_b64_e32 v[12:13], v[2:3]
	v_mov_b64_e32 v[14:15], v[2:3]
	v_mov_b64_e32 v[16:17], v[2:3]
	v_mov_b64_e32 v[18:19], v[2:3]
	v_mov_b64_e32 v[20:21], v[2:3]
	v_mov_b64_e32 v[22:23], v[2:3]
	v_mov_b64_e32 v[24:25], v[2:3]
	v_mov_b64_e32 v[26:27], v[2:3]
	v_mov_b64_e32 v[28:29], v[2:3]
	v_mov_b64_e32 v[30:31], v[2:3]
	v_mov_b64_e32 v[32:33], v[2:3]
	v_mov_b64_e32 v[34:35], v[2:3]
	v_mov_b64_e32 v[36:37], v[2:3]
	v_mov_b64_e32 v[38:39], v[2:3]
	v_mov_b64_e32 v[40:41], v[2:3]
	v_mov_b64_e32 v[42:43], v[2:3]
	v_mov_b64_e32 v[44:45], v[2:3]
	v_mov_b64_e32 v[46:47], v[2:3]
	v_mov_b64_e32 v[48:49], v[2:3]
	v_mov_b64_e32 v[50:51], v[2:3]
	v_mov_b64_e32 v[52:53], v[2:3]
	v_mov_b64_e32 v[54:55], v[2:3]
	v_mov_b64_e32 v[56:57], v[2:3]
	v_mov_b64_e32 v[58:59], v[2:3]
	v_mov_b64_e32 v[60:61], v[2:3]
	v_mov_b64_e32 v[62:63], v[2:3]
	v_mov_b64_e32 v[64:65], v[2:3]
	v_mov_b64_e32 v[66:67], v[2:3]
	v_mov_b64_e32 v[68:69], v[2:3]
	v_mov_b64_e32 v[70:71], v[2:3]
	v_mov_b64_e32 v[72:73], v[2:3]
	v_mov_b64_e32 v[74:75], v[2:3]
	v_mov_b64_e32 v[76:77], v[2:3]
	v_mov_b64_e32 v[78:79], v[2:3]
	v_mov_b64_e32 v[80:81], v[2:3]
	v_mov_b64_e32 v[82:83], v[2:3]
	v_mov_b64_e32 v[84:85], v[2:3]
	v_mov_b64_e32 v[86:87], v[2:3]
	v_mov_b64_e32 v[88:89], v[2:3]
	v_mov_b64_e32 v[90:91], v[2:3]
	v_mov_b64_e32 v[92:93], v[2:3]
	v_mov_b64_e32 v[94:95], v[2:3]
	v_mov_b64_e32 v[96:97], v[2:3]
	v_mov_b64_e32 v[98:99], v[2:3]
	v_mov_b64_e32 v[100:101], v[2:3]
	v_mov_b64_e32 v[102:103], v[2:3]
	v_mov_b64_e32 v[104:105], v[2:3]
	v_mov_b64_e32 v[106:107], v[2:3]
	v_mov_b64_e32 v[108:109], v[2:3]
	v_mov_b64_e32 v[110:111], v[2:3]
	v_mov_b64_e32 v[112:113], v[2:3]
	v_mov_b64_e32 v[114:115], v[2:3]
	v_mov_b64_e32 v[116:117], v[2:3]
	v_mov_b64_e32 v[118:119], v[2:3]
	v_mov_b64_e32 v[120:121], v[2:3]
	v_mov_b64_e32 v[122:123], v[2:3]
	v_mov_b64_e32 v[124:125], v[2:3]
	v_mov_b64_e32 v[126:127], v[2:3]
	v_mov_b64_e32 v[128:129], v[2:3]

;     ...
;             const char* a1 = cA + (size_t)(t + 1) * kstep;
;             const char* a2 = last ? nA : cA + (size_t)(t + 2) * kstep; const char* b2 = last ? nB : cB + (size_t)(t + 2) * kstep;
;             const char* a3 = a2 + kstep; const char* b3 = b2 + kstep;
;     ...
;         for (int a = 0; a < 2; ++a)
; #pragma unroll
;             for (int b = 0; b < 2; ++b)
; #pragma unroll
;                 for (int m = 0; m < 4; ++m)
; #pragma unroll
;                     for (int n = 0; n < 2; ++n) acc[a][b][m][n] = (f32x4){0.f, 0.f, 0.f, 0.f};
;         cur = nxt; cA = nA; cB = nB; ++ui;
.LBB0_3369:
	s_add_u32 s14, s14, 0xb0080
	s_addc_u32 s15, s15, 0
	s_add_u32 s0, s16, 0x100
	v_mov_b32_e32 v2, 0
	s_addc_u32 s45, s17, 0
	s_mov_b32 s46, -2
	v_mov_b32_e32 v3, v2
	v_mov_b64_e32 v[4:5], v[2:3]
	v_mov_b64_e32 v[6:7], v[2:3]
	v_mov_b64_e32 v[8:9], v[2:3]
	v_mov_b64_e32 v[10:11], v[2:3]
	v_mov_b64_e32 v[12:13], v[2:3]
	v_mov_b64_e32 v[14:15], v[2:3]
	v_mov_b64_e32 v[16:17], v[2:3]
	v_mov_b64_e32 v[18:19], v[2:3]
	v_mov_b64_e32 v[20:21], v[2:3]
	v_mov_b64_e32 v[22:23], v[2:3]
	v_mov_b64_e32 v[24:25], v[2:3]
	v_mov_b64_e32 v[26:27], v[2:3]
	v_mov_b64_e32 v[28:29], v[2:3]
	v_mov_b64_e32 v[30:31], v[2:3]
	v_mov_b64_e32 v[32:33], v[2:3]
	v_mov_b64_e32 v[34:35], v[2:3]
	v_mov_b64_e32 v[36:37], v[2:3]
	v_mov_b64_e32 v[38:39], v[2:3]
	v_mov_b64_e32 v[40:41], v[2:3]
	v_mov_b64_e32 v[42:43], v[2:3]
	v_mov_b64_e32 v[44:45], v[2:3]
	v_mov_b64_e32 v[46:47], v[2:3]
	v_mov_b64_e32 v[48:49], v[2:3]
	v_mov_b64_e32 v[50:51], v[2:3]
	v_mov_b64_e32 v[52:53], v[2:3]
	v_mov_b64_e32 v[54:55], v[2:3]
	v_mov_b64_e32 v[56:57], v[2:3]
	v_mov_b64_e32 v[58:59], v[2:3]
	v_mov_b64_e32 v[60:61], v[2:3]
	v_mov_b64_e32 v[62:63], v[2:3]
	v_mov_b64_e32 v[64:65], v[2:3]
	v_mov_b64_e32 v[66:67], v[2:3]
	v_mov_b64_e32 v[68:69], v[2:3]
	v_mov_b64_e32 v[70:71], v[2:3]
	v_mov_b64_e32 v[72:73], v[2:3]
	v_mov_b64_e32 v[74:75], v[2:3]
	v_mov_b64_e32 v[76:77], v[2:3]
	v_mov_b64_e32 v[78:79], v[2:3]
	v_mov_b64_e32 v[80:81], v[2:3]
	v_mov_b64_e32 v[82:83], v[2:3]
	v_mov_b64_e32 v[84:85], v[2:3]
	v_mov_b64_e32 v[86:87], v[2:3]
	v_mov_b64_e32 v[88:89], v[2:3]
	v_mov_b64_e32 v[90:91], v[2:3]
	v_mov_b64_e32 v[92:93], v[2:3]
	v_mov_b64_e32 v[94:95], v[2:3]
	v_mov_b64_e32 v[96:97], v[2:3]
	v_mov_b64_e32 v[98:99], v[2:3]
	v_mov_b64_e32 v[100:101], v[2:3]
	v_mov_b64_e32 v[102:103], v[2:3]
	v_mov_b64_e32 v[104:105], v[2:3]
	v_mov_b64_e32 v[106:107], v[2:3]
	v_mov_b64_e32 v[108:109], v[2:3]
	v_mov_b64_e32 v[110:111], v[2:3]
	v_mov_b64_e32 v[112:113], v[2:3]
	v_mov_b64_e32 v[114:115], v[2:3]
	v_mov_b64_e32 v[116:117], v[2:3]
	v_mov_b64_e32 v[118:119], v[2:3]
	v_mov_b64_e32 v[120:121], v[2:3]
	v_mov_b64_e32 v[122:123], v[2:3]
	v_mov_b64_e32 v[124:125], v[2:3]
	v_mov_b64_e32 v[126:127], v[2:3]
	v_mov_b64_e32 v[128:129], v[2:3]

;     ...
;         for (int a = 0; a < 2; ++a)
; #pragma unroll
;             for (int b = 0; b < 2; ++b)
; #pragma unroll
;                 for (int m = 0; m < 4; ++m)
; #pragma unroll
;                     for (int n = 0; n < 2; ++n) acc[a][b][m][n] = (f32x4){0.f, 0.f, 0.f, 0.f};
;         cur = nxt; cA = nA; cB = nB; ++ui;
.LBB0_3555:
	s_ashr_i32 s17, s16, 31
	s_lshl_b64 s[20:21], s[16:17], 19
	s_cmpk_gt_i32 s14, 0x3e7
	s_cselect_b32 s15, s28, s30
	s_cselect_b32 s0, s29, s31
	s_add_u32 s20, s15, s20
	s_addc_u32 s21, s0, s21
	s_and_b64 s[26:27], s[26:27], exec
	s_cselect_b32 s0, s21, s25
	s_cselect_b32 s15, s20, s24
	s_add_u32 s22, s22, 0x40080
	s_addc_u32 s23, s23, 0
	s_add_u32 s17, s24, 0x100
	v_mov_b32_e32 v2, 0
	s_addc_u32 s47, s25, 0
	s_mov_b32 s48, -2
	v_mov_b32_e32 v3, v2
	v_mov_b64_e32 v[4:5], v[2:3]
	v_mov_b64_e32 v[6:7], v[2:3]
	v_mov_b64_e32 v[8:9], v[2:3]
	v_mov_b64_e32 v[10:11], v[2:3]
	v_mov_b64_e32 v[12:13], v[2:3]
	v_mov_b64_e32 v[14:15], v[2:3]
	v_mov_b64_e32 v[16:17], v[2:3]
	v_mov_b64_e32 v[18:19], v[2:3]
	v_mov_b64_e32 v[20:21], v[2:3]
	v_mov_b64_e32 v[22:23], v[2:3]
	v_mov_b64_e32 v[24:25], v[2:3]
	v_mov_b64_e32 v[26:27], v[2:3]
	v_mov_b64_e32 v[28:29], v[2:3]
	v_mov_b64_e32 v[30:31], v[2:3]
	v_mov_b64_e32 v[32:33], v[2:3]
	v_mov_b64_e32 v[34:35], v[2:3]
	v_mov_b64_e32 v[36:37], v[2:3]
	v_mov_b64_e32 v[38:39], v[2:3]
	v_mov_b64_e32 v[40:41], v[2:3]
	v_mov_b64_e32 v[42:43], v[2:3]
	v_mov_b64_e32 v[44:45], v[2:3]
	v_mov_b64_e32 v[46:47], v[2:3]
	v_mov_b64_e32 v[48:49], v[2:3]
	v_mov_b64_e32 v[50:51], v[2:3]
	v_mov_b64_e32 v[52:53], v[2:3]
	v_mov_b64_e32 v[54:55], v[2:3]
	v_mov_b64_e32 v[56:57], v[2:3]
	v_mov_b64_e32 v[58:59], v[2:3]
	v_mov_b64_e32 v[60:61], v[2:3]
	v_mov_b64_e32 v[62:63], v[2:3]
	v_mov_b64_e32 v[64:65], v[2:3]
	v_mov_b64_e32 v[66:67], v[2:3]
	v_mov_b64_e32 v[68:69], v[2:3]
	v_mov_b64_e32 v[70:71], v[2:3]
	v_mov_b64_e32 v[72:73], v[2:3]
	v_mov_b64_e32 v[74:75], v[2:3]
	v_mov_b64_e32 v[76:77], v[2:3]
	v_mov_b64_e32 v[78:79], v[2:3]
	v_mov_b64_e32 v[80:81], v[2:3]
	v_mov_b64_e32 v[82:83], v[2:3]
	v_mov_b64_e32 v[84:85], v[2:3]
	v_mov_b64_e32 v[86:87], v[2:3]
	v_mov_b64_e32 v[88:89], v[2:3]
	v_mov_b64_e32 v[90:91], v[2:3]
	v_mov_b64_e32 v[92:93], v[2:3]
	v_mov_b64_e32 v[94:95], v[2:3]
	v_mov_b64_e32 v[96:97], v[2:3]
	v_mov_b64_e32 v[98:99], v[2:3]
	v_mov_b64_e32 v[100:101], v[2:3]
	v_mov_b64_e32 v[102:103], v[2:3]
	v_mov_b64_e32 v[104:105], v[2:3]
	v_mov_b64_e32 v[106:107], v[2:3]
	v_mov_b64_e32 v[108:109], v[2:3]
	v_mov_b64_e32 v[110:111], v[2:3]
	v_mov_b64_e32 v[112:113], v[2:3]
	v_mov_b64_e32 v[114:115], v[2:3]
	v_mov_b64_e32 v[116:117], v[2:3]
	v_mov_b64_e32 v[118:119], v[2:3]
	v_mov_b64_e32 v[120:121], v[2:3]
	v_mov_b64_e32 v[122:123], v[2:3]
	v_mov_b64_e32 v[124:125], v[2:3]
	v_mov_b64_e32 v[126:127], v[2:3]
	v_mov_b64_e32 v[128:129], v[2:3]

;     __device__ __forceinline__ bool next(int i, Unit& u) const { return unit_of((long)i * G + c, u); }
;     __device__ __forceinline__ bool next(int i, Unit& u) const { if (i >= 64) return false; return unit_of((long)__builtin_amdgcn_readfirstlane(list[i]), u); }
;     ...
;         const bool has_next = S.next(ui + 1, nxt);
;         const char* nA = has_next ? S.a_base(nxt) : cA; const char* nB = has_next ? S.b_base(nxt) : cB;
;         for (int t = 0; t < nt; t += 2) {
;             const bool last = (t == nt - 2);
;             const char* a1 = cA + (size_t)(t + 1) * kstep;
;             const char* a2 = last ? nA : cA + (size_t)(t + 2) * kstep; const char* b2 = last ? nB : cB + (size_t)(t + 2) * kstep;
;             const char* a3 = a2 + kstep; const char* b3 = b2 + kstep;
;     ...
;         for (int a = 0; a < 2; ++a)
; #pragma unroll
;             for (int b = 0; b < 2; ++b)
; #pragma unroll
;                 for (int m = 0; m < 4; ++m)
; #pragma unroll
;                     for (int n = 0; n < 2; ++n) acc[a][b][m][n] = (f32x4){0.f, 0.f, 0.f, 0.f};
;         cur = nxt; cA = nA; cB = nB; ++ui;
.LBB0_4201:
	s_ashr_i32 s13, s12, 31
	s_lshl_b64 s[14:15], s[12:13], 19
	s_add_u32 s14, s27, s14
	s_addc_u32 s15, s28, s15
	s_and_b64 s[16:17], s[0:1], exec
	s_cselect_b32 s13, s15, s21
	s_cselect_b32 s19, s14, s20
	s_ashr_i32 s11, s10, 31
	s_lshl_b64 s[16:17], s[10:11], 19
	s_add_u32 s16, s29, s16
	s_addc_u32 s17, s30, s17
	s_and_b64 s[24:25], s[0:1], exec
	s_cselect_b32 s11, s17, s23
	s_cselect_b32 s49, s16, s22
	s_add_u32 s20, s20, 0x40080
	s_addc_u32 s21, s21, 0
	s_add_u32 s50, s22, 0x100
	v_mov_b32_e32 v2, 0
	s_addc_u32 s51, s23, 0
	s_mov_b32 s52, -2
	v_mov_b32_e32 v3, v2
	v_mov_b64_e32 v[4:5], v[2:3]
	v_mov_b64_e32 v[6:7], v[2:3]
	v_mov_b64_e32 v[8:9], v[2:3]
	v_mov_b64_e32 v[10:11], v[2:3]
	v_mov_b64_e32 v[12:13], v[2:3]
	v_mov_b64_e32 v[14:15], v[2:3]
	v_mov_b64_e32 v[16:17], v[2:3]
	v_mov_b64_e32 v[18:19], v[2:3]
	v_mov_b64_e32 v[20:21], v[2:3]
	v_mov_b64_e32 v[22:23], v[2:3]
	v_mov_b64_e32 v[24:25], v[2:3]
	v_mov_b64_e32 v[26:27], v[2:3]
	v_mov_b64_e32 v[28:29], v[2:3]
	v_mov_b64_e32 v[30:31], v[2:3]
	v_mov_b64_e32 v[32:33], v[2:3]
	v_mov_b64_e32 v[34:35], v[2:3]
	v_mov_b64_e32 v[36:37], v[2:3]
	v_mov_b64_e32 v[38:39], v[2:3]
	v_mov_b64_e32 v[40:41], v[2:3]
	v_mov_b64_e32 v[42:43], v[2:3]
	v_mov_b64_e32 v[44:45], v[2:3]
	v_mov_b64_e32 v[46:47], v[2:3]
	v_mov_b64_e32 v[48:49], v[2:3]
	v_mov_b64_e32 v[50:51], v[2:3]
	v_mov_b64_e32 v[52:53], v[2:3]
	v_mov_b64_e32 v[54:55], v[2:3]
	v_mov_b64_e32 v[56:57], v[2:3]
	v_mov_b64_e32 v[58:59], v[2:3]
	v_mov_b64_e32 v[60:61], v[2:3]
	v_mov_b64_e32 v[62:63], v[2:3]
	v_mov_b64_e32 v[64:65], v[2:3]
	v_mov_b64_e32 v[66:67], v[2:3]
	v_mov_b64_e32 v[68:69], v[2:3]
	v_mov_b64_e32 v[70:71], v[2:3]
	v_mov_b64_e32 v[72:73], v[2:3]
	v_mov_b64_e32 v[74:75], v[2:3]
	v_mov_b64_e32 v[76:77], v[2:3]
	v_mov_b64_e32 v[78:79], v[2:3]
	v_mov_b64_e32 v[80:81], v[2:3]
	v_mov_b64_e32 v[82:83], v[2:3]
	v_mov_b64_e32 v[84:85], v[2:3]
	v_mov_b64_e32 v[86:87], v[2:3]
	v_mov_b64_e32 v[88:89], v[2:3]
	v_mov_b64_e32 v[90:91], v[2:3]
	v_mov_b64_e32 v[92:93], v[2:3]
	v_mov_b64_e32 v[94:95], v[2:3]
	v_mov_b64_e32 v[96:97], v[2:3]
	v_mov_b64_e32 v[98:99], v[2:3]
	v_mov_b64_e32 v[100:101], v[2:3]
	v_mov_b64_e32 v[102:103], v[2:3]
	v_mov_b64_e32 v[104:105], v[2:3]
	v_mov_b64_e32 v[106:107], v[2:3]
	v_mov_b64_e32 v[108:109], v[2:3]
	v_mov_b64_e32 v[110:111], v[2:3]
	v_mov_b64_e32 v[112:113], v[2:3]
	v_mov_b64_e32 v[114:115], v[2:3]
	v_mov_b64_e32 v[116:117], v[2:3]
	v_mov_b64_e32 v[118:119], v[2:3]
	v_mov_b64_e32 v[120:121], v[2:3]
	v_mov_b64_e32 v[122:123], v[2:3]
	v_mov_b64_e32 v[124:125], v[2:3]
	v_mov_b64_e32 v[126:127], v[2:3]
	v_mov_b64_e32 v[128:129], v[2:3]

;     ...
;             const char* a1 = cA + (size_t)(t + 1) * kstep;
;             const char* a2 = last ? nA : cA + (size_t)(t + 2) * kstep; const char* b2 = last ? nB : cB + (size_t)(t + 2) * kstep;
;             const char* a3 = a2 + kstep; const char* b3 = b2 + kstep;
;     ...
;         for (int a = 0; a < 2; ++a)
; #pragma unroll
;             for (int b = 0; b < 2; ++b)
; #pragma unroll
;                 for (int m = 0; m < 4; ++m)
; #pragma unroll
;                     for (int n = 0; n < 2; ++n) acc[a][b][m][n] = (f32x4){0.f, 0.f, 0.f, 0.f};
;         cur = nxt; cA = nA; cB = nB; ++ui;
.LBB0_4504:
	s_add_u32 s50, s50, 0xe0080
	v_lshl_add_u64 v[164:165], v[2:3], 0, s[30:31]
	v_mov_b32_e32 v2, 0
	s_addc_u32 s51, s51, 0
	s_mov_b32 s83, -2
	v_mov_b32_e32 v3, v2
	v_mov_b64_e32 v[4:5], v[2:3]
	v_mov_b64_e32 v[6:7], v[2:3]
	v_mov_b64_e32 v[8:9], v[2:3]
	v_mov_b64_e32 v[10:11], v[2:3]
	v_mov_b64_e32 v[12:13], v[2:3]
	v_mov_b64_e32 v[14:15], v[2:3]
	v_mov_b64_e32 v[16:17], v[2:3]
	v_mov_b64_e32 v[18:19], v[2:3]
	v_mov_b64_e32 v[20:21], v[2:3]
	v_mov_b64_e32 v[22:23], v[2:3]
	v_mov_b64_e32 v[24:25], v[2:3]
	v_mov_b64_e32 v[26:27], v[2:3]
	v_mov_b64_e32 v[28:29], v[2:3]
	v_mov_b64_e32 v[30:31], v[2:3]
	v_mov_b64_e32 v[32:33], v[2:3]
	v_mov_b64_e32 v[34:35], v[2:3]
	v_mov_b64_e32 v[36:37], v[2:3]
	v_mov_b64_e32 v[38:39], v[2:3]
	v_mov_b64_e32 v[40:41], v[2:3]
	v_mov_b64_e32 v[42:43], v[2:3]
	v_mov_b64_e32 v[44:45], v[2:3]
	v_mov_b64_e32 v[46:47], v[2:3]
	v_mov_b64_e32 v[48:49], v[2:3]
	v_mov_b64_e32 v[50:51], v[2:3]
	v_mov_b64_e32 v[52:53], v[2:3]
	v_mov_b64_e32 v[54:55], v[2:3]
	v_mov_b64_e32 v[56:57], v[2:3]
	v_mov_b64_e32 v[58:59], v[2:3]
	v_mov_b64_e32 v[60:61], v[2:3]
	v_mov_b64_e32 v[62:63], v[2:3]
	v_mov_b64_e32 v[64:65], v[2:3]
	v_mov_b64_e32 v[66:67], v[2:3]
	v_mov_b64_e32 v[68:69], v[2:3]
	v_mov_b64_e32 v[70:71], v[2:3]
	v_mov_b64_e32 v[72:73], v[2:3]
	v_mov_b64_e32 v[74:75], v[2:3]
	v_mov_b64_e32 v[76:77], v[2:3]
	v_mov_b64_e32 v[78:79], v[2:3]
	v_mov_b64_e32 v[80:81], v[2:3]
	v_mov_b64_e32 v[82:83], v[2:3]
	v_mov_b64_e32 v[84:85], v[2:3]
	v_mov_b64_e32 v[86:87], v[2:3]
	v_mov_b64_e32 v[88:89], v[2:3]
	v_mov_b64_e32 v[90:91], v[2:3]
	v_mov_b64_e32 v[92:93], v[2:3]
	v_mov_b64_e32 v[94:95], v[2:3]
	v_mov_b64_e32 v[96:97], v[2:3]
	v_mov_b64_e32 v[98:99], v[2:3]
	v_mov_b64_e32 v[100:101], v[2:3]
	v_mov_b64_e32 v[102:103], v[2:3]
	v_mov_b64_e32 v[104:105], v[2:3]
	v_mov_b64_e32 v[106:107], v[2:3]
	v_mov_b64_e32 v[108:109], v[2:3]
	v_mov_b64_e32 v[110:111], v[2:3]
	v_mov_b64_e32 v[112:113], v[2:3]
	v_mov_b64_e32 v[114:115], v[2:3]
	v_mov_b64_e32 v[116:117], v[2:3]
	v_mov_b64_e32 v[118:119], v[2:3]
	v_mov_b64_e32 v[120:121], v[2:3]
	v_mov_b64_e32 v[122:123], v[2:3]
	v_mov_b64_e32 v[124:125], v[2:3]
	v_mov_b64_e32 v[126:127], v[2:3]
	v_mov_b64_e32 v[128:129], v[2:3]

;     __device__ __forceinline__ bool next(int i, Unit& u) const { return unit_of((long)i * G + c, u); }
;     __device__ __forceinline__ bool next(int i, Unit& u) const { if (i >= 64) return false; return unit_of((long)__builtin_amdgcn_readfirstlane(list[i]), u); }
;     ...
;         const bool has_next = S.next(ui + 1, nxt);
;         const char* nA = has_next ? S.a_base(nxt) : cA; const char* nB = has_next ? S.b_base(nxt) : cB;
;         for (int t = 0; t < nt; t += 2) {
;             const bool last = (t == nt - 2);
;             const char* a1 = cA + (size_t)(t + 1) * kstep;
;             const char* a2 = last ? nA : cA + (size_t)(t + 2) * kstep; const char* b2 = last ? nB : cB + (size_t)(t + 2) * kstep;
;             const char* a3 = a2 + kstep; const char* b3 = b2 + kstep;
;     ...
;         for (int a = 0; a < 2; ++a)
; #pragma unroll
;             for (int b = 0; b < 2; ++b)
; #pragma unroll
;                 for (int m = 0; m < 4; ++m)
; #pragma unroll
;                     for (int n = 0; n < 2; ++n) acc[a][b][m][n] = (f32x4){0.f, 0.f, 0.f, 0.f};
;         cur = nxt; cA = nA; cB = nB; ++ui;
.LBB0_4533:
	s_ashr_i32 s51, s50, 31
	s_lshl_b64 s[42:43], s[50:51], 19
	s_add_u32 s42, s72, s42
	s_addc_u32 s43, s73, s43
	s_and_b64 s[56:57], s[56:57], exec
	s_cselect_b32 s3, s43, s55
	s_cselect_b32 s51, s42, s54
	s_add_u32 s54, s54, 0x40080
	v_lshl_add_u64 v[164:165], v[2:3], 0, s[30:31]
	v_mov_b32_e32 v2, 0
	s_addc_u32 s55, s55, 0
	s_mov_b32 s80, -2
	v_mov_b32_e32 v3, v2
	v_mov_b64_e32 v[4:5], v[2:3]
	v_mov_b64_e32 v[6:7], v[2:3]
	v_mov_b64_e32 v[8:9], v[2:3]
	v_mov_b64_e32 v[10:11], v[2:3]
	v_mov_b64_e32 v[12:13], v[2:3]
	v_mov_b64_e32 v[14:15], v[2:3]
	v_mov_b64_e32 v[16:17], v[2:3]
	v_mov_b64_e32 v[18:19], v[2:3]
	v_mov_b64_e32 v[20:21], v[2:3]
	v_mov_b64_e32 v[22:23], v[2:3]
	v_mov_b64_e32 v[24:25], v[2:3]
	v_mov_b64_e32 v[26:27], v[2:3]
	v_mov_b64_e32 v[28:29], v[2:3]
	v_mov_b64_e32 v[30:31], v[2:3]
	v_mov_b64_e32 v[32:33], v[2:3]
	v_mov_b64_e32 v[34:35], v[2:3]
	v_mov_b64_e32 v[36:37], v[2:3]
	v_mov_b64_e32 v[38:39], v[2:3]
	v_mov_b64_e32 v[40:41], v[2:3]
	v_mov_b64_e32 v[42:43], v[2:3]
	v_mov_b64_e32 v[44:45], v[2:3]
	v_mov_b64_e32 v[46:47], v[2:3]
	v_mov_b64_e32 v[48:49], v[2:3]
	v_mov_b64_e32 v[50:51], v[2:3]
	v_mov_b64_e32 v[52:53], v[2:3]
	v_mov_b64_e32 v[54:55], v[2:3]
	v_mov_b64_e32 v[56:57], v[2:3]
	v_mov_b64_e32 v[58:59], v[2:3]
	v_mov_b64_e32 v[60:61], v[2:3]
	v_mov_b64_e32 v[62:63], v[2:3]
	v_mov_b64_e32 v[64:65], v[2:3]
	v_mov_b64_e32 v[66:67], v[2:3]
	v_mov_b64_e32 v[68:69], v[2:3]
	v_mov_b64_e32 v[70:71], v[2:3]
	v_mov_b64_e32 v[72:73], v[2:3]
	v_mov_b64_e32 v[74:75], v[2:3]
	v_mov_b64_e32 v[76:77], v[2:3]
	v_mov_b64_e32 v[78:79], v[2:3]
	v_mov_b64_e32 v[80:81], v[2:3]
	v_mov_b64_e32 v[82:83], v[2:3]
	v_mov_b64_e32 v[84:85], v[2:3]
	v_mov_b64_e32 v[86:87], v[2:3]
	v_mov_b64_e32 v[88:89], v[2:3]
	v_mov_b64_e32 v[90:91], v[2:3]
	v_mov_b64_e32 v[92:93], v[2:3]
	v_mov_b64_e32 v[94:95], v[2:3]
	v_mov_b64_e32 v[96:97], v[2:3]
	v_mov_b64_e32 v[98:99], v[2:3]
	v_mov_b64_e32 v[100:101], v[2:3]
	v_mov_b64_e32 v[102:103], v[2:3]
	v_mov_b64_e32 v[104:105], v[2:3]
	v_mov_b64_e32 v[106:107], v[2:3]
	v_mov_b64_e32 v[108:109], v[2:3]
	v_mov_b64_e32 v[110:111], v[2:3]
	v_mov_b64_e32 v[112:113], v[2:3]
	v_mov_b64_e32 v[114:115], v[2:3]
	v_mov_b64_e32 v[116:117], v[2:3]
	v_mov_b64_e32 v[118:119], v[2:3]
	v_mov_b64_e32 v[120:121], v[2:3]
	v_mov_b64_e32 v[122:123], v[2:3]
	v_mov_b64_e32 v[124:125], v[2:3]
	v_mov_b64_e32 v[126:127], v[2:3]
	v_mov_b64_e32 v[128:129], v[2:3]
